# baseline (speedup 1.0000x reference)
.LBB1_62:
	v_min_f32_e64 v32, |v80|, |v96|
	s_nop 0
	v_min3_f32 v32, v32, |v81|, |v97|
	v_min3_f32 v32, v32, |v82|, |v98|
	v_min3_f32 v32, v32, |v83|, |v99|
	v_min3_f32 v32, v32, |v84|, |v100|
	v_min3_f32 v32, v32, |v85|, |v101|
	v_min3_f32 v32, v32, |v86|, |v102|
	v_min3_f32 v32, v32, |v87|, |v103|
	v_min3_f32 v32, v32, |v88|, |v104|
	v_min3_f32 v32, v32, |v89|, |v105|
	v_min3_f32 v32, v32, |v90|, |v106|
	v_min3_f32 v32, v32, |v91|, |v107|
	v_min3_f32 v32, v32, |v92|, |v108|
	v_min3_f32 v32, v32, |v93|, |v109|
	v_min3_f32 v32, v32, |v94|, |v110|
	v_min3_f32 v32, v32, |v95|, |v111|
	v_cmp_eq_f32_e32 vcc, 0, v32
	s_cbranch_vccnz .LBB1_84

.LBB1_64:
	v_add_f32_e32 v49, v49, v48
	v_max_f32_e32 v48, v50, v51
	v_max3_f32 v78, v52, v53, v33
	v_max3_f32 v48, v48, v32, v34
	v_max3_f32 v48, v48, v35, v54
	v_max3_f32 v78, v78, v56, v57
	v_max3_f32 v48, v48, v55, v36
	v_max3_f32 v78, v78, v38, v39
	v_max3_f32 v48, v48, v37, v58
	v_max3_f32 v78, v78, v60, v61
	v_max3_f32 v48, v48, v59, v40
	v_max3_f32 v78, v78, v42, v43
	v_max3_f32 v48, v48, v41, v62
	v_max3_f32 v78, v78, v64, v65
	v_max3_f32 v48, v48, v63, v44
	v_max3_f32 v78, v78, v46, v47
	v_max3_f32 v48, v48, v45, v78
	v_mov_b32_e32 v78, v48
	s_nop 1
	v_permlane32_swap_b32_e32 v48, v78
	v_max_f32_e32 v48, v48, v78
	v_cmp_lt_f32_e32 vcc, s34, v48
	s_cmp_lg_u64 vcc, 0
	s_cselect_b64 s[20:21], -1, 0
	s_cbranch_vccnz .LBB1_77

.LBB1_71:
	v_add_f32_e32 v49, v49, v48
	v_max_f32_e32 v48, v64, v65
	v_max3_f32 v66, v62, v63, v33
	v_max3_f32 v48, v48, v32, v34
	v_max3_f32 v48, v48, v35, v68
	v_max3_f32 v66, v66, v70, v71
	v_max3_f32 v48, v48, v69, v36
	v_max3_f32 v66, v66, v38, v39
	v_max3_f32 v48, v48, v37, v72
	v_max3_f32 v66, v66, v74, v75
	v_max3_f32 v48, v48, v73, v40
	v_max3_f32 v66, v66, v42, v43
	v_max3_f32 v48, v48, v41, v76
	v_max3_f32 v66, v66, v78, v79
	v_max3_f32 v48, v48, v77, v44
	v_max3_f32 v66, v66, v46, v47
	v_max3_f32 v48, v48, v45, v66
	v_mov_b32_e32 v66, v48
	s_nop 1
	v_permlane32_swap_b32_e32 v48, v66
	v_max_f32_e32 v48, v48, v66
	v_cmp_lt_f32_e32 vcc, s34, v48
	s_cmp_lg_u64 vcc, 0
	s_cselect_b64 s[18:19], -1, 0
	s_cbranch_vccnz .LBB1_81

.LBB1_74:
	s_add_i32 s4, s20, 0x4000
	s_cmpk_lg_u32 s20, 0x8000
	s_cselect_b32 s4, s4, 0
	s_add_i32 s18, s36, 2
	s_cmp_le_u32 s36, s33
	v_lshl_add_u64 v[180:181], v[180:181], 0, s[8:9]
	s_cbranch_scc0 .LBB1_89
	s_mov_b32 s36, s18
	s_mov_b32 s30, s28
	s_mov_b32 s35, s20
	s_mov_b32 s28, s4
	s_branch .LBB1_60
	s_nop 0
	s_nop 0
	s_nop 0
	s_nop 0
	s_nop 0
	s_nop 0
	s_nop 0
	s_nop 0
	s_nop 0
	s_nop 0
	s_nop 0
	s_nop 0
